# spatial-gating unit: u/z gate operands fetched as 8 coalesced 16-byte loads per wave, staged in a private LDS slab and read back per lane (replaces 64 four-byte global loads per wave)
# baseline (speedup 1.0000x reference)
; __device__ __forceinline__ int crow(int r, int hi) { return (r & 3) + 8 * (r >> 2) + 4 * hi; }
; __device__ __forceinline__ void unit(const bf16_t* proj, const float* stats  , const float* lng, const float* lnb, const float* sw, const float* sb, bf16_t* Y2, int un, LAS unsigned char* lds) {
;     ...
;     f32x4 wv[16]; unsigned uu[32], zq[32]; float bias[16];
; #pragma unroll
;     for (int i = 0; i < 8; ++i) { const int s0 = (i >> 2) * 64 + 16 * (i & 3) + hi * 8; const float* wp = sw + ((size_t)g * 128 + t) * 128 + s0; wv[2 * i] = *(const f32x4*)wp; wv[2 * i + 1] = *(const f32x4*)(wp + 4); }
; #pragma unroll
;     for (int r = 0; r < 16; ++r) { const int tr = tb * 32 + att::crow(r, hi), bt = R0 + tr; bias[r] = sb[g * 128 + tr];
; #pragma unroll
;         for (int d = 0; d < 2; ++d) { const int ch = g * 128 + (2 * eh + d) * 32 + (r32 & ~1); uu[r * 2 + d] = *(const unsigned*)(proj + (size_t)bt * NC + C_UC + ch); zq[r * 2 + d] = *(const unsigned*)(proj + (size_t)bt * NC + C_ZC + ch); } }
.LBB0_1376:
	s_andn2_b64 vcc, exec, s[0:1]
	s_cbranch_vccnz .LBB0_425
	v_readlane_b32 s4, v252, 35
	v_readlane_b32 s10, v252, 41
	v_readlane_b32 s11, v252, 42
	s_mov_b64 s[0:1], s[10:11]
	v_readlane_b32 s5, v252, 36
	v_readlane_b32 s12, v252, 43
	v_readlane_b32 s13, v252, 44
	v_readlane_b32 s10, v254, 43
	v_readlane_b32 s11, v254, 44
	s_add_u32 s0, s0, s10
	s_mov_b64 s[4:5], s[12:13]
	s_addc_u32 s1, s1, s11
	v_readlane_b32 s6, v252, 37
	v_readlane_b32 s7, v252, 38
	v_readlane_b32 s8, v252, 39
	v_readlane_b32 s9, v252, 40
	v_readlane_b32 s14, v252, 45
	v_readlane_b32 s15, v252, 46
	s_add_u32 s4, s4, s10
	s_addc_u32 s5, s5, s11
	s_mov_b64 s[6:7], s[14:15]
	v_readlane_b32 s8, v253, 54
	v_readlane_b32 s16, v252, 47
	v_readlane_b32 s17, v252, 48
	v_readlane_b32 s9, v253, 55
	s_add_u32 s12, s6, s8
	s_addc_u32 s13, s7, s9
	s_mov_b64 s[6:7], s[16:17]
	s_add_u32 s6, s6, s10
	v_readlane_b32 s8, v254, 47
	s_addc_u32 s7, s7, s11
	s_waitcnt vmcnt(23)
	v_mov_b32_e32 v176, v0
	s_and_b32 s2, s8, 7
	s_lshl_b32 s8, s8, 4
	s_add_i32 s8, s8, 0x7fffe000
	v_readfirstlane_b32 s10, v176
	s_and_b32 s11, s8, 0x7fffff80
	s_lshr_b32 s8, s10, 1
	v_and_b32_e32 v177, 31, v176
	s_and_b32 s9, s8, 0x60
	v_or_b32_e32 v182, s9, v177
	s_lshl_b32 s8, s2, 16
	s_waitcnt vmcnt(3)
	v_lshl_or_b32 v2, v182, 9, s8
	v_lshl_add_u64 v[4:5], s[12:13], 0, v[2:3]
	v_and_b32_e32 v2, 32, v176
	s_lshl_b32 s2, s2, 7
	s_ashr_i32 s8, s10, 2
	v_lshl_add_u64 v[40:41], v[4:5], 0, v[2:3]
	s_andn2_b32 s8, s8, 63
	v_and_or_b32 v2, v176, 30, s2
	s_waitcnt vmcnt(0)
	v_bfe_u32 v1, v176, 5, 1
	v_add_u32_e32 v68, s8, v2
	v_readlane_b32 s12, v253, 48
	v_lshlrev_b32_e32 v183, 3, v1
	v_lshl_or_b32 v1, v1, 2, s9
	v_ashrrev_i32_e32 v69, 31, v68
	v_readlane_b32 s13, v253, 49
	v_or_b32_e32 v2, s11, v1
	s_mov_b32 s14, 0xe800
	v_mov_b64_e32 v[100:101], s[12:13]
	v_lshlrev_b64 v[84:85], 1, v[68:69]
	v_or_b32_e32 v68, 32, v68
	v_readlane_b32 s18, v252, 49
	v_readlane_b32 s19, v252, 50
	v_mad_u64_u32 v[70:71], s[12:13], v2, s14, v[100:101]
	s_mov_b64 s[16:17], 0x4000
	v_ashrrev_i32_e32 v69, 31, v68
	v_lshl_add_u64 v[72:73], v[70:71], 0, s[16:17]
	s_mov_b64 s[18:19], 0x5000
	v_lshlrev_b64 v[86:87], 1, v[68:69]
	v_lshl_add_u64 v[70:71], v[70:71], 0, s[18:19]
	v_lshl_add_u64 v[74:75], v[72:73], 0, v[84:85]
	v_lshl_add_u64 v[68:69], v[72:73], 0, v[86:87]
	global_load_dwordx4 v[28:31], v[40:41], off offset:16
	global_load_dwordx4 v[32:35], v[40:41], off
	global_load_dwordx4 v[20:23], v[40:41], off offset:80
	global_load_dwordx4 v[24:27], v[40:41], off offset:64
	s_cmp_ge_u32 s9, 32
	s_cselect_b64 exec, -1, 0
	global_load_dwordx4 v[12:15], v[40:41], off offset:144
	global_load_dwordx4 v[16:19], v[40:41], off offset:128
	s_waitcnt lgkmcnt(0)
	global_load_dwordx4 v[4:7], v[40:41], off offset:208
	global_load_dwordx4 v[8:11], v[40:41], off offset:192
	s_cmp_ge_u32 s9, 64
	s_cselect_b64 exec, -1, 0
	global_load_dwordx4 v[60:63], v[40:41], off offset:272
	global_load_dwordx4 v[64:67], v[40:41], off offset:256
	global_load_dwordx4 v[52:55], v[40:41], off offset:336
	global_load_dwordx4 v[56:59], v[40:41], off offset:320
	s_cmp_ge_u32 s9, 0x60
	s_cselect_b64 exec, -1, 0
	global_load_dwordx4 v[44:47], v[40:41], off offset:400
	global_load_dwordx4 v[48:51], v[40:41], off offset:384
	global_load_dwordx4 v[36:39], v[40:41], off offset:464
	s_nop 0
	global_load_dwordx4 v[40:43], v[40:41], off offset:448
	s_mov_b64 exec, -1
	v_or_b32_e32 v1, s2, v1
	v_bfe_u32 v160, v176, 3, 3
	v_or_b32_e32 v160, s9, v160
	v_or_b32_e32 v160, s11, v160
	v_mad_u64_u32 v[162:163], s[12:13], v160, s14, v[100:101]
	v_and_b32_e32 v160, 7, v176
	v_lshlrev_b32_e32 v160, 4, v160
	s_add_i32 s100, s2, s8
	s_lshl_b32 s100, s100, 1
	v_add_u32_e32 v160, s100, v160
	v_mov_b32_e32 v161, 0
	v_lshl_add_u64 v[162:163], v[162:163], 0, v[160:161]
	v_lshl_add_u64 v[162:163], v[162:163], 0, s[16:17]
	s_mov_b32 s100, 0x800
	s_mov_b32 s101, 0
	v_lshl_add_u64 v[162:163], v[162:163], 0, s[100:101]
	s_mov_b32 s100, 0x74000
	global_load_dwordx4 v[120:123], v[162:163], off offset:-2048
	global_load_dwordx4 v[136:139], v[162:163], off offset:2048
	v_lshl_add_u64 v[162:163], v[162:163], 0, s[100:101]
	global_load_dwordx4 v[124:127], v[162:163], off offset:-2048
	global_load_dwordx4 v[140:143], v[162:163], off offset:2048
	v_lshl_add_u64 v[162:163], v[162:163], 0, s[100:101]
	global_load_dwordx4 v[128:131], v[162:163], off offset:-2048
	global_load_dwordx4 v[148:151], v[162:163], off offset:2048
	v_lshl_add_u64 v[162:163], v[162:163], 0, s[100:101]
	global_load_dwordx4 v[132:135], v[162:163], off offset:-2048
	global_load_dwordx4 v[152:155], v[162:163], off offset:2048
	v_lshl_add_u64 v[74:75], v[70:71], 0, v[84:85]
	v_lshl_add_u64 v[68:69], v[70:71], 0, v[86:87]
	v_or_b32_e32 v68, 1, v2
	v_mad_u64_u32 v[68:69], s[12:13], v68, s14, v[100:101]
	v_lshl_add_u64 v[70:71], v[68:69], 0, s[16:17]
	v_lshl_add_u64 v[68:69], v[68:69], 0, s[18:19]
	v_lshl_add_u64 v[72:73], v[70:71], 0, v[84:85]
	v_lshl_add_u64 v[70:71], v[70:71], 0, v[86:87]
	v_lshl_add_u64 v[72:73], v[68:69], 0, v[84:85]
	v_lshl_add_u64 v[68:69], v[68:69], 0, v[86:87]
	v_or_b32_e32 v68, 2, v2
	v_mad_u64_u32 v[68:69], s[12:13], v68, s14, v[100:101]
	v_lshl_add_u64 v[70:71], v[68:69], 0, s[16:17]
	v_lshl_add_u64 v[68:69], v[68:69], 0, s[18:19]
	v_lshl_add_u64 v[72:73], v[70:71], 0, v[84:85]
	v_lshl_add_u64 v[70:71], v[70:71], 0, v[86:87]
	v_lshl_add_u64 v[72:73], v[68:69], 0, v[84:85]
	v_lshl_add_u64 v[68:69], v[68:69], 0, v[86:87]
	v_or_b32_e32 v68, 3, v2
	v_mad_u64_u32 v[68:69], s[12:13], v68, s14, v[100:101]
	v_lshl_add_u64 v[70:71], v[68:69], 0, s[16:17]
	v_lshl_add_u64 v[68:69], v[68:69], 0, s[18:19]
; __device__ __forceinline__ int crow(int r, int hi) { return (r & 3) + 8 * (r >> 2) + 4 * hi; }
; __device__ __forceinline__ void unit(const bf16_t* proj, const float* stats  , const float* lng, const float* lnb, const float* sw, const float* sb, bf16_t* Y2, int un, LAS unsigned char* lds) {
;     ...
;     for (int r = 0; r < 16; ++r) { const int tr = tb * 32 + att::crow(r, hi), bt = R0 + tr; bias[r] = sb[g * 128 + tr];
; #pragma unroll
;         for (int d = 0; d < 2; ++d) { const int ch = g * 128 + (2 * eh + d) * 32 + (r32 & ~1); uu[r * 2 + d] = *(const unsigned*)(proj + (size_t)bt * NC + C_UC + ch); zq[r * 2 + d] = *(const unsigned*)(proj + (size_t)bt * NC + C_ZC + ch); } }
;     { const int sr = tid >> 4, sc = (tid & 15) * 8, ch = g * 128 + sc;
;       const f32x4 g0 = *(const f32x4*)(lng + ch), g1 = *(const f32x4*)(lng + ch + 4), b0 = *(const f32x4*)(lnb + ch), b1 = *(const f32x4*)(lnb + ch + 4);
;       float mus[4], rss[4];
;       { float2 pp[4];
; #pragma unroll
;         for (int q = 0; q < 4; ++q) pp[q] = *(const float2*)(stats + ((size_t)(R0 + sr + 32 * q) * 16 + (tid & 15)) * 2);
	v_lshl_add_u64 v[72:73], v[70:71], 0, v[84:85]
	v_lshl_add_u64 v[70:71], v[70:71], 0, v[86:87]
	v_lshl_add_u64 v[72:73], v[68:69], 0, v[84:85]
	v_lshl_add_u64 v[68:69], v[68:69], 0, v[86:87]
	v_or_b32_e32 v68, 8, v2
	v_mad_u64_u32 v[68:69], s[12:13], v68, s14, v[100:101]
	v_lshl_add_u64 v[70:71], v[68:69], 0, s[16:17]
	v_lshl_add_u64 v[68:69], v[68:69], 0, s[18:19]
	v_lshl_add_u64 v[72:73], v[70:71], 0, v[84:85]
	v_lshl_add_u64 v[70:71], v[70:71], 0, v[86:87]
	v_lshl_add_u64 v[72:73], v[68:69], 0, v[84:85]
	v_lshl_add_u64 v[68:69], v[68:69], 0, v[86:87]
	v_or_b32_e32 v68, 9, v2
	v_mad_u64_u32 v[68:69], s[12:13], v68, s14, v[100:101]
	v_lshl_add_u64 v[70:71], v[68:69], 0, s[16:17]
	v_lshl_add_u64 v[68:69], v[68:69], 0, s[18:19]
	v_lshl_add_u64 v[72:73], v[70:71], 0, v[84:85]
	v_lshl_add_u64 v[70:71], v[70:71], 0, v[86:87]
	v_lshl_add_u64 v[72:73], v[68:69], 0, v[84:85]
	v_lshl_add_u64 v[68:69], v[68:69], 0, v[86:87]
	v_or_b32_e32 v68, 10, v2
	v_mad_u64_u32 v[68:69], s[12:13], v68, s14, v[100:101]
	v_lshl_add_u64 v[70:71], v[68:69], 0, s[16:17]
	v_lshl_add_u64 v[68:69], v[68:69], 0, s[18:19]
	v_lshl_add_u64 v[72:73], v[70:71], 0, v[84:85]
	v_lshl_add_u64 v[70:71], v[70:71], 0, v[86:87]
	v_lshl_add_u64 v[72:73], v[68:69], 0, v[84:85]
	v_lshl_add_u64 v[68:69], v[68:69], 0, v[86:87]
	v_or_b32_e32 v68, 11, v2
	v_mad_u64_u32 v[68:69], s[12:13], v68, s14, v[100:101]
	v_lshl_add_u64 v[70:71], v[68:69], 0, s[16:17]
	v_lshl_add_u64 v[68:69], v[68:69], 0, s[18:19]
	v_lshl_add_u64 v[72:73], v[70:71], 0, v[84:85]
	v_lshl_add_u64 v[70:71], v[70:71], 0, v[86:87]
	v_lshl_add_u64 v[72:73], v[68:69], 0, v[84:85]
	v_lshl_add_u64 v[68:69], v[68:69], 0, v[86:87]
	v_or_b32_e32 v68, 16, v2
	v_mad_u64_u32 v[68:69], s[12:13], v68, s14, v[100:101]
	v_lshl_add_u64 v[70:71], v[68:69], 0, s[16:17]
	v_lshl_add_u64 v[68:69], v[68:69], 0, s[18:19]
	v_lshl_add_u64 v[88:89], v[70:71], 0, v[84:85]
	v_lshl_add_u64 v[88:89], v[68:69], 0, v[84:85]
	v_lshl_add_u64 v[70:71], v[70:71], 0, v[86:87]
	v_lshl_add_u64 v[68:69], v[68:69], 0, v[86:87]
	v_or_b32_e32 v68, 17, v2
	v_mad_u64_u32 v[68:69], s[12:13], v68, s14, v[100:101]
	v_lshl_add_u64 v[70:71], v[68:69], 0, s[16:17]
	v_lshl_add_u64 v[68:69], v[68:69], 0, s[18:19]
	v_lshl_add_u64 v[88:89], v[70:71], 0, v[84:85]
	v_lshl_add_u64 v[70:71], v[70:71], 0, v[86:87]
	v_lshl_add_u64 v[88:89], v[68:69], 0, v[84:85]
	v_lshl_add_u64 v[68:69], v[68:69], 0, v[86:87]
	v_or_b32_e32 v68, 18, v2
	v_mad_u64_u32 v[68:69], s[12:13], v68, s14, v[100:101]
	v_lshl_add_u64 v[70:71], v[68:69], 0, s[16:17]
	v_lshl_add_u64 v[68:69], v[68:69], 0, s[18:19]
	v_lshl_add_u64 v[88:89], v[70:71], 0, v[84:85]
	v_lshl_add_u64 v[70:71], v[70:71], 0, v[86:87]
	v_lshl_add_u64 v[88:89], v[68:69], 0, v[84:85]
	v_lshl_add_u64 v[68:69], v[68:69], 0, v[86:87]
	v_or_b32_e32 v68, 19, v2
	v_mad_u64_u32 v[68:69], s[12:13], v68, s14, v[100:101]
	v_lshl_add_u64 v[70:71], v[68:69], 0, s[16:17]
	v_lshl_add_u64 v[68:69], v[68:69], 0, s[18:19]
	v_lshl_add_u64 v[88:89], v[70:71], 0, v[84:85]
	v_lshl_add_u64 v[70:71], v[70:71], 0, v[86:87]
	v_lshl_add_u64 v[88:89], v[68:69], 0, v[84:85]
	v_lshlrev_b32_e32 v1, 2, v1
	v_lshl_add_u64 v[68:69], v[68:69], 0, v[86:87]
	v_or_b32_e32 v88, 24, v2
	global_load_dwordx4 v[80:83], v1, s[6:7]
	global_load_dwordx4 v[76:79], v1, s[6:7] offset:32
	global_load_dwordx4 v[72:75], v1, s[6:7] offset:64
	v_ashrrev_i32_e32 v185, 4, v176
	global_load_dwordx4 v[68:71], v1, s[6:7] offset:96
	v_mad_u64_u32 v[88:89], s[6:7], v88, s14, v[100:101]
	v_lshl_add_u64 v[90:91], v[88:89], 0, s[16:17]
	v_lshl_add_u64 v[88:89], v[88:89], 0, s[18:19]
	v_lshl_add_u64 v[92:93], v[90:91], 0, v[84:85]
	v_lshl_add_u64 v[90:91], v[90:91], 0, v[86:87]
	v_lshl_add_u64 v[92:93], v[88:89], 0, v[84:85]
	v_lshl_add_u64 v[88:89], v[88:89], 0, v[86:87]
	v_or_b32_e32 v1, 25, v2
	v_mad_u64_u32 v[88:89], s[6:7], v1, s14, v[100:101]
	v_lshl_add_u64 v[90:91], v[88:89], 0, s[16:17]
	v_lshl_add_u64 v[88:89], v[88:89], 0, s[18:19]
	v_lshl_add_u64 v[92:93], v[90:91], 0, v[84:85]
	v_lshl_add_u64 v[90:91], v[90:91], 0, v[86:87]
	v_lshl_add_u64 v[92:93], v[88:89], 0, v[84:85]
	v_lshl_add_u64 v[88:89], v[88:89], 0, v[86:87]
	v_or_b32_e32 v1, 26, v2
	v_mad_u64_u32 v[88:89], s[6:7], v1, s14, v[100:101]
	v_lshl_add_u64 v[90:91], v[88:89], 0, s[16:17]
	v_lshl_add_u64 v[88:89], v[88:89], 0, s[18:19]
	v_lshl_add_u64 v[92:93], v[90:91], 0, v[84:85]
	v_lshl_add_u64 v[90:91], v[90:91], 0, v[86:87]
	v_lshl_add_u64 v[92:93], v[88:89], 0, v[84:85]
	v_lshl_add_u64 v[88:89], v[88:89], 0, v[86:87]
	v_or_b32_e32 v1, 27, v2
	v_mad_u64_u32 v[88:89], s[6:7], v1, s14, v[100:101]
	v_lshl_add_u64 v[90:91], v[88:89], 0, s[16:17]
	v_lshl_add_u64 v[88:89], v[88:89], 0, s[18:19]
	v_lshl_add_u64 v[92:93], v[90:91], 0, v[84:85]
	v_lshl_add_u64 v[84:85], v[88:89], 0, v[84:85]
	v_lshl_add_u64 v[84:85], v[90:91], 0, v[86:87]
	v_lshl_add_u64 v[84:85], v[88:89], 0, v[86:87]
	v_and_b32_e32 v84, 15, v176
	v_lshlrev_b32_e32 v102, 3, v84
	v_or_b32_e32 v191, s2, v102
	v_lshlrev_b32_e32 v96, 2, v191
	global_load_dwordx4 v[84:87], v96, s[0:1] offset:16
	global_load_dwordx4 v[92:95], v96, s[0:1]
	global_load_dwordx4 v[88:91], v96, s[4:5] offset:16
	s_nop 0
	global_load_dwordx4 v[96:99], v96, s[4:5]
	v_add_u32_e32 v110, s11, v185
	v_readlane_b32 s0, v254, 37
	v_mov_b32_e32 v103, v3
	v_readlane_b32 s1, v254, 38
	v_ashrrev_i32_e32 v111, 31, v110
	v_lshlrev_b64 v[104:105], 7, v[110:111]
	v_lshl_add_u64 v[102:103], s[0:1], 0, v[102:103]
	v_lshl_add_u64 v[112:113], v[102:103], 0, v[104:105]
	global_load_dwordx2 v[104:105], v[112:113], off
	s_movk_i32 s0, 0x2000
	v_add_co_u32_e32 v116, vcc, s0, v112
	s_movk_i32 s0, 0x3000
	s_nop 0
	v_addc_co_u32_e32 v117, vcc, 0, v113, vcc
	global_load_dwordx2 v[102:103], v[116:117], off offset:-4096
	global_load_dwordx2 v[186:187], v[116:117], off
	v_add_co_u32_e32 v112, vcc, s0, v112
	v_and_b32_e32 v106, 64, v229
	s_nop 0
	v_addc_co_u32_e32 v113, vcc, 0, v113, vcc
	v_add_u32_e32 v106, 64, v106
	v_xor_b32_e32 v108, 1, v229
	v_cmp_lt_i32_e32 vcc, v108, v106
	global_load_dwordx2 v[188:189], v[112:113], off
	s_mov_b32 s0, 0x3a800000
	v_cndmask_b32_e32 v108, v229, v108, vcc
	v_lshlrev_b32_e32 v145, 2, v108
	v_xor_b32_e32 v108, 2, v229
	v_cmp_lt_i32_e32 vcc, v108, v106
	s_movk_i32 s4, 0x4000
	v_and_b32_e32 v184, 63, v176
	v_cndmask_b32_e32 v108, v229, v108, vcc
	v_lshlrev_b32_e32 v111, 2, v108
	v_xor_b32_e32 v108, 4, v229
	v_cmp_lt_i32_e32 vcc, v108, v106
	s_cmpk_gt_u32 s10, 0xff
	s_waitcnt vmcnt(3)
; __device__ __forceinline__ int crow(int r, int hi) { return (r & 3) + 8 * (r >> 2) + 4 * hi; }
; __device__ __forceinline__ void unit(const bf16_t* proj, const float* stats  , const float* lng, const float* lnb, const float* sw, const float* sb, bf16_t* Y2, int un, LAS unsigned char* lds) {
;     ...
;     for (int r = 0; r < 16; ++r) { const int tr = tb * 32 + att::crow(r, hi), bt = R0 + tr; bias[r] = sb[g * 128 + tr];
; #pragma unroll
;         for (int d = 0; d < 2; ++d) { const int ch = g * 128 + (2 * eh + d) * 32 + (r32 & ~1); uu[r * 2 + d] = *(const unsigned*)(proj + (size_t)bt * NC + C_UC + ch); zq[r * 2 + d] = *(const unsigned*)(proj + (size_t)bt * NC + C_ZC + ch); } }
;     ...
;         for (int q = 0; q < 4; ++q) { float s1 = pp[q].x, s2 = pp[q].y;
; #pragma unroll
;             for (int off = 1; off < 16; off <<= 1) { s1 += __shfl_xor(s1, off); s2 += __shfl_xor(s2, off); }
;             mus[q] = s1 * (1.0f / 1024.0f); rss[q] = __builtin_amdgcn_rsqf(fmaxf(s2 * (1.0f / 1024.0f) - mus[q] * mus[q], 0.f) + LN_EPS); } }
	v_and_b32_e32 v160, 63, v176
	v_lshlrev_b32_e32 v160, 4, v160
	v_lshrrev_b32_e32 v161, 6, v176
	v_lshl_add_u32 v160, v161, 13, v160
	v_add_u32_e32 v160, 0x10000, v160
	ds_write_b128 v160, v[120:123] offset:0
	ds_write_b128 v160, v[136:139] offset:4096
	ds_write_b128 v160, v[124:127] offset:1024
	ds_write_b128 v160, v[140:143] offset:5120
	ds_write_b128 v160, v[128:131] offset:2048
	ds_write_b128 v160, v[148:151] offset:6144
	ds_write_b128 v160, v[132:135] offset:3072
	ds_write_b128 v160, v[152:155] offset:7168
	v_and_b32_e32 v162, 30, v176
	v_lshlrev_b32_e32 v162, 1, v162
	v_bfe_u32 v163, v176, 5, 1
	v_lshl_add_u32 v162, v163, 9, v162
	v_lshl_add_u32 v162, v161, 13, v162
	v_add_u32_e32 v162, 0x10000, v162
	ds_read_b32 v180, v162 offset:0
	ds_read_b32 v178, v162 offset:64
	ds_read_b32 v181, v162 offset:4096
	ds_read_b32 v179, v162 offset:4160
	ds_read_b32 v173, v162 offset:128
	ds_read_b32 v172, v162 offset:192
	ds_read_b32 v174, v162 offset:4288
	ds_read_b32 v175, v162 offset:4224
	ds_read_b32 v170, v162 offset:256
	ds_read_b32 v168, v162 offset:320
	ds_read_b32 v169, v162 offset:4416
	ds_read_b32 v171, v162 offset:4352
	ds_read_b32 v165, v162 offset:384
	ds_read_b32 v164, v162 offset:448
	ds_read_b32 v166, v162 offset:4544
	ds_read_b32 v167, v162 offset:4480
	ds_read_b32 v157, v162 offset:1152
	ds_read_b32 v156, v162 offset:1216
	ds_read_b32 v158, v162 offset:5312
	ds_read_b32 v159, v162 offset:5248
	ds_read_b32 v154, v162 offset:1280
	ds_read_b32 v152, v162 offset:1344
	ds_read_b32 v153, v162 offset:5440
	ds_read_b32 v155, v162 offset:5376
	ds_read_b32 v149, v162 offset:1408
	ds_read_b32 v148, v162 offset:1472
	ds_read_b32 v150, v162 offset:5568
	ds_read_b32 v151, v162 offset:5504
	ds_read_b32 v146, v162 offset:2048
	ds_read_b32 v143, v162 offset:2112
	ds_read_b32 v144, v162 offset:6208
	ds_read_b32 v147, v162 offset:6144
	ds_read_b32 v140, v162 offset:2176
	ds_read_b32 v139, v162 offset:2240
	ds_read_b32 v141, v162 offset:6336
	ds_read_b32 v142, v162 offset:6272
	ds_read_b32 v137, v162 offset:2304
	ds_read_b32 v135, v162 offset:2368
	ds_read_b32 v136, v162 offset:6464
	ds_read_b32 v138, v162 offset:6400
	ds_read_b32 v133, v162 offset:2432
	ds_read_b32 v131, v162 offset:2496
	ds_read_b32 v134, v162 offset:6528
	ds_read_b32 v132, v162 offset:6592
	ds_read_b32 v129, v162 offset:3072
	ds_read_b32 v127, v162 offset:3136
	ds_read_b32 v128, v162 offset:7232
	ds_read_b32 v130, v162 offset:7168
	ds_read_b32 v125, v162 offset:3200
	ds_read_b32 v123, v162 offset:3264
	ds_read_b32 v124, v162 offset:7360
	ds_read_b32 v126, v162 offset:7296
	ds_read_b32 v121, v162 offset:3328
	ds_read_b32 v119, v162 offset:3392
	ds_read_b32 v120, v162 offset:7488
	ds_read_b32 v122, v162 offset:7424
	ds_read_b32 v109, v162 offset:3456
	ds_read_b32 v115, v162 offset:7552
	ds_read_b32 v1, v162 offset:3520
	ds_read_b32 v107, v162 offset:7616
	ds_read_b32 v160, v162 offset:1088
	ds_read_b32 v161, v162 offset:5184
	ds_read_b32 v163, v162 offset:5120
	ds_read_b32 v162, v162 offset:1024
	ds_bpermute_b32 v112, v145, v104
	ds_bpermute_b32 v113, v145, v105
	v_cndmask_b32_e32 v108, v229, v108, vcc
	v_lshlrev_b32_e32 v190, 2, v108
	v_xor_b32_e32 v108, 8, v229
	v_cmp_lt_i32_e32 vcc, v108, v106
	s_waitcnt lgkmcnt(0)
	v_pk_add_f32 v[104:105], v[104:105], v[112:113]
	ds_bpermute_b32 v112, v111, v104
	ds_bpermute_b32 v113, v111, v105
	v_cndmask_b32_e32 v106, v229, v108, vcc
	v_lshlrev_b32_e32 v106, 2, v106
	s_waitcnt lgkmcnt(0)
	v_pk_add_f32 v[104:105], v[104:105], v[112:113]
	ds_bpermute_b32 v112, v190, v104
	ds_bpermute_b32 v113, v190, v105
	s_waitcnt lgkmcnt(0)
	v_pk_add_f32 v[104:105], v[104:105], v[112:113]
	ds_bpermute_b32 v112, v106, v104
	ds_bpermute_b32 v113, v106, v105
	s_waitcnt lgkmcnt(0)
	v_pk_add_f32 v[104:105], v[104:105], v[112:113]
	s_nop 0
	v_pk_mul_f32 v[116:117], v[104:105], s[0:1] op_sel_hi:[1,0]
	s_waitcnt vmcnt(2)
	ds_bpermute_b32 v105, v145, v103
	v_fma_f32 v104, -v116, v116, v117
	v_max_f32_e32 v104, 0, v104
	v_add_f32_e32 v104, 0x3727c5ac, v104
	v_rsq_f32_e32 v118, v104
	ds_bpermute_b32 v104, v145, v102
	s_waitcnt lgkmcnt(0)
	v_pk_add_f32 v[102:103], v[102:103], v[104:105]
	ds_bpermute_b32 v104, v111, v102
	ds_bpermute_b32 v105, v111, v103
	s_waitcnt lgkmcnt(0)
	v_pk_add_f32 v[102:103], v[102:103], v[104:105]
	ds_bpermute_b32 v104, v190, v102
	ds_bpermute_b32 v105, v190, v103
	s_waitcnt lgkmcnt(0)
	v_pk_add_f32 v[102:103], v[102:103], v[104:105]
	ds_bpermute_b32 v104, v106, v102
	ds_bpermute_b32 v105, v106, v103
	s_waitcnt lgkmcnt(0)
	v_pk_add_f32 v[102:103], v[102:103], v[104:105]
	s_nop 0
	v_pk_mul_f32 v[112:113], v[102:103], s[0:1] op_sel_hi:[1,0]
	s_waitcnt vmcnt(1)
	ds_bpermute_b32 v103, v145, v187
	v_fma_f32 v102, -v112, v112, v113
	v_max_f32_e32 v102, 0, v102
	v_add_f32_e32 v102, 0x3727c5ac, v102
	v_rsq_f32_e32 v114, v102
	ds_bpermute_b32 v102, v145, v186
	s_waitcnt lgkmcnt(0)
	v_pk_add_f32 v[102:103], v[186:187], v[102:103]
	ds_bpermute_b32 v104, v111, v102
	ds_bpermute_b32 v105, v111, v103
	s_waitcnt lgkmcnt(0)
	v_pk_add_f32 v[102:103], v[102:103], v[104:105]
	ds_bpermute_b32 v104, v190, v102
	ds_bpermute_b32 v105, v190, v103
	s_waitcnt lgkmcnt(0)
	v_pk_add_f32 v[102:103], v[102:103], v[104:105]
	ds_bpermute_b32 v104, v106, v102
	ds_bpermute_b32 v105, v106, v103
	s_waitcnt lgkmcnt(0)
	v_pk_add_f32 v[102:103], v[102:103], v[104:105]
	s_nop 0
	v_pk_mul_f32 v[102:103], v[102:103], s[0:1] op_sel_hi:[1,0]
	s_waitcnt vmcnt(0)
	ds_bpermute_b32 v105, v145, v189
	v_fma_f32 v104, -v102, v102, v103
	v_max_f32_e32 v104, 0, v104
	v_add_f32_e32 v104, 0x3727c5ac, v104
	v_rsq_f32_e32 v108, v104
	ds_bpermute_b32 v104, v145, v188
	s_waitcnt lgkmcnt(0)
; __device__ __forceinline__ unsigned cvt_pk_bf16(float lo, float hi) { f32x2_t v = {lo, hi}; bf16x2_t b = __builtin_convertvector(v, bf16x2_t); return __builtin_bit_cast(unsigned, b); }
; #define LAS __attribute__((address_space(3)))
; __device__ __forceinline__ float bflo(unsigned w) { return __uint_as_float(w << 16); }
; __device__ __forceinline__ float bfhi(unsigned w) { return __uint_as_float(w & 0xffff0000u); }
; __device__ __forceinline__ int v_st(int k, int c) { const int kk = (k & ~0xC) | ((k & 4) << 1) | ((k & 8) >> 1); return ((kk >> 3) * 4 + (c >> 5)) * 512 + ((kk & 7) * 32 + (c & 31)) * 2; }
; __device__ __forceinline__ void unit(const bf16_t* proj, const float* stats  , const float* lng, const float* lnb, const float* sw, const float* sb, bf16_t* Y2, int un, LAS unsigned char* lds) {
;     ...
;         for (int q = 0; q < 4; ++q) { float s1 = pp[q].x, s2 = pp[q].y;
; #pragma unroll
;             for (int off = 1; off < 16; off <<= 1) { s1 += __shfl_xor(s1, off); s2 += __shfl_xor(s2, off); }
;             mus[q] = s1 * (1.0f / 1024.0f); rss[q] = __builtin_amdgcn_rsqf(fmaxf(s2 * (1.0f / 1024.0f) - mus[q] * mus[q], 0.f) + LN_EPS); } }
; #pragma unroll
;       for (int q = 0; q < 4; ++q) { const int s = sr + 32 * q, row = R0 + s; const u32x4 vv = *(const u32x4*)(proj + (size_t)row * NC + C_VC + ch);
;           const float mu = mus[q], rs = rss[q];
;           u32x4 w; w.x = pg8::cvt_pk_bf16((bflo(vv.x) - mu) * rs * g0[0] + b0[0], (bfhi(vv.x) - mu) * rs * g0[1] + b0[1]); w.y = pg8::cvt_pk_bf16((bflo(vv.y) - mu) * rs * g0[2] + b0[2], (bfhi(vv.y) - mu) * rs * g0[3] + b0[3]);
;           w.z = pg8::cvt_pk_bf16((bflo(vv.z) - mu) * rs * g1[0] + b1[0], (bfhi(vv.z) - mu) * rs * g1[1] + b1[1]); w.w = pg8::cvt_pk_bf16((bflo(vv.w) - mu) * rs * g1[2] + b1[2], (bfhi(vv.w) - mu) * rs * g1[3] + b1[3]);
;           *(LAS u32x4*)(lds + (s >> 6) * att::SHM_V + att::v_st(s & 63, sc)) = w; } }
	v_pk_add_f32 v[104:105], v[188:189], v[104:105]
	ds_bpermute_b32 v186, v111, v104
	ds_bpermute_b32 v187, v111, v105
	v_lshlrev_b32_e32 v111, 1, v185
	v_bfe_u32 v188, v176, 2, 2
	s_waitcnt lgkmcnt(0)
	v_pk_add_f32 v[104:105], v[104:105], v[186:187]
	ds_bpermute_b32 v186, v190, v104
	ds_bpermute_b32 v187, v190, v105
	s_waitcnt lgkmcnt(0)
	v_pk_add_f32 v[104:105], v[104:105], v[186:187]
	ds_bpermute_b32 v186, v106, v104
	ds_bpermute_b32 v187, v106, v105
	s_waitcnt lgkmcnt(0)
	v_pk_add_f32 v[104:105], v[104:105], v[186:187]
	v_and_b32_e32 v187, 8, v111
	v_lshrrev_b32_e32 v111, 1, v185
	v_and_b32_e32 v186, 3, v185
	v_and_or_b32 v111, v111, 4, v186
	v_pk_mul_f32 v[104:105], v[104:105], s[0:1] op_sel_hi:[1,0]
	v_lshlrev_b32_e32 v189, 6, v111
	v_mad_i64_i32 v[192:193], s[0:1], v110, s14, v[100:101]
	v_lshlrev_b32_e32 v110, 1, v191
	v_mov_b32_e32 v111, v3
	v_lshl_add_u64 v[192:193], v[192:193], 0, v[110:111]
	v_add_co_u32_e32 v192, vcc, s4, v192
	v_lshlrev_b32_e32 v186, 4, v176
	s_nop 0
	v_addc_co_u32_e32 v193, vcc, 0, v193, vcc
	global_load_dwordx4 v[196:199], v[192:193], off offset:2048
	v_and_b32_e32 v190, 48, v186
	v_fma_f32 v106, -v104, v104, v105
	v_max_f32_e32 v106, 0, v106
	v_add_f32_e32 v106, 0x3727c5ac, v106
	v_rsq_f32_e32 v106, v106
	s_waitcnt vmcnt(0)
	v_lshlrev_b32_e32 v192, 16, v196
	v_and_b32_e32 v193, 0xffff0000, v196
	v_pk_add_f32 v[192:193], v[192:193], v[116:117] op_sel_hi:[1,0] neg_lo:[0,1] neg_hi:[0,1]
	s_nop 0
	v_pk_mul_f32 v[192:193], v[118:119], v[192:193] op_sel_hi:[0,1]
	v_pk_fma_f32 v[192:193], v[92:93], v[192:193], v[96:97]
	s_nop 0
	v_cvt_pk_bf16_f32 v196, v192, v193
	v_lshlrev_b32_e32 v192, 16, v197
	v_and_b32_e32 v193, 0xffff0000, v197
	v_pk_add_f32 v[192:193], v[192:193], v[116:117] op_sel_hi:[1,0] neg_lo:[0,1] neg_hi:[0,1]
	s_nop 0
	v_pk_mul_f32 v[192:193], v[118:119], v[192:193] op_sel_hi:[0,1]
	v_pk_fma_f32 v[192:193], v[94:95], v[192:193], v[98:99]
	s_nop 0
	v_cvt_pk_bf16_f32 v197, v192, v193
	v_lshlrev_b32_e32 v192, 16, v198
	v_and_b32_e32 v193, 0xffff0000, v198
	v_pk_add_f32 v[192:193], v[192:193], v[116:117] op_sel_hi:[1,0] neg_lo:[0,1] neg_hi:[0,1]
	s_nop 0
	v_pk_mul_f32 v[192:193], v[118:119], v[192:193] op_sel_hi:[0,1]
	v_pk_fma_f32 v[192:193], v[84:85], v[192:193], v[88:89]
	s_nop 0
	v_cvt_pk_bf16_f32 v198, v192, v193
	v_lshlrev_b32_e32 v192, 16, v199
	v_and_b32_e32 v193, 0xffff0000, v199
	v_pk_add_f32 v[116:117], v[192:193], v[116:117] op_sel_hi:[1,0] neg_lo:[0,1] neg_hi:[0,1]
	s_nop 0
	v_pk_mul_f32 v[116:117], v[118:119], v[116:117] op_sel_hi:[0,1]
	v_pk_fma_f32 v[116:117], v[86:87], v[116:117], v[90:91]
	s_nop 0
	v_cvt_pk_bf16_f32 v199, v116, v117
	v_lshlrev_b32_e32 v116, 8, v185
	v_and_b32_e32 v117, 0xffffc000, v116
	v_and_or_b32 v116, v185, 48, v187
	v_lshrrev_b32_e32 v116, 1, v116
	v_or_b32_e32 v116, v116, v188
	v_lshlrev_b32_e32 v116, 9, v116
	v_add3_u32 v117, 0, v117, v116
	v_add3_u32 v117, v117, v189, v190
	ds_write_b128 v117, v[196:199]
	v_add_u32_e32 v117, 32, v185
	v_add_u32_e32 v118, s11, v117
	v_mad_i64_i32 v[192:193], s[0:1], v118, s14, v[100:101]
	v_lshl_add_u64 v[192:193], v[192:193], 0, v[110:111]
	v_add_co_u32_e32 v192, vcc, s4, v192
	s_nop 1
	v_addc_co_u32_e32 v193, vcc, 0, v193, vcc
	global_load_dwordx4 v[196:199], v[192:193], off offset:2048
	s_waitcnt vmcnt(0)
	v_lshlrev_b32_e32 v192, 16, v196
	v_and_b32_e32 v193, 0xffff0000, v196
	v_pk_add_f32 v[192:193], v[192:193], v[112:113] op_sel_hi:[1,0] neg_lo:[0,1] neg_hi:[0,1]
	s_nop 0
	v_pk_mul_f32 v[192:193], v[114:115], v[192:193] op_sel_hi:[0,1]
	v_pk_fma_f32 v[192:193], v[92:93], v[192:193], v[96:97]
	s_nop 0
	v_cvt_pk_bf16_f32 v196, v192, v193
	v_lshlrev_b32_e32 v192, 16, v197
	v_and_b32_e32 v193, 0xffff0000, v197
	v_pk_add_f32 v[192:193], v[192:193], v[112:113] op_sel_hi:[1,0] neg_lo:[0,1] neg_hi:[0,1]
	s_nop 0
	v_pk_mul_f32 v[192:193], v[114:115], v[192:193] op_sel_hi:[0,1]
	v_pk_fma_f32 v[192:193], v[94:95], v[192:193], v[98:99]
	s_nop 0
	v_cvt_pk_bf16_f32 v197, v192, v193
	v_lshlrev_b32_e32 v192, 16, v198
	v_and_b32_e32 v193, 0xffff0000, v198
	v_pk_add_f32 v[192:193], v[192:193], v[112:113] op_sel_hi:[1,0] neg_lo:[0,1] neg_hi:[0,1]
	s_nop 0
	v_pk_mul_f32 v[192:193], v[114:115], v[192:193] op_sel_hi:[0,1]
	v_pk_fma_f32 v[192:193], v[84:85], v[192:193], v[88:89]
	s_nop 0
	v_cvt_pk_bf16_f32 v198, v192, v193
	v_lshlrev_b32_e32 v192, 16, v199
	v_and_b32_e32 v193, 0xffff0000, v199
	v_pk_add_f32 v[112:113], v[192:193], v[112:113] op_sel_hi:[1,0] neg_lo:[0,1] neg_hi:[0,1]
	s_nop 0
	v_pk_mul_f32 v[112:113], v[114:115], v[112:113] op_sel_hi:[0,1]
	v_pk_fma_f32 v[112:113], v[86:87], v[112:113], v[90:91]
	v_add_u32_e32 v114, 64, v185
	v_cvt_pk_bf16_f32 v199, v112, v113
	v_and_or_b32 v113, v117, 48, v187
	v_lshrrev_b32_e32 v113, 1, v113
	v_lshlrev_b32_e32 v112, 8, v117
	v_or_b32_e32 v113, v113, v188
	v_and_b32_e32 v112, 0xffffc000, v112
	v_lshlrev_b32_e32 v113, 9, v113
	v_add3_u32 v112, 0, v112, v113
	v_add3_u32 v112, v112, v189, v190
	ds_write_b128 v112, v[196:199]
	v_add_u32_e32 v112, s11, v114
	v_mad_i64_i32 v[112:113], s[0:1], v112, s14, v[100:101]
	v_lshl_add_u64 v[112:113], v[112:113], 0, v[110:111]
	v_add_co_u32_e32 v112, vcc, s4, v112
	s_nop 1
	v_addc_co_u32_e32 v113, vcc, 0, v113, vcc
	global_load_dwordx4 v[196:199], v[112:113], off offset:2048
	s_waitcnt vmcnt(0)
; __device__ __forceinline__ unsigned cvt_pk_bf16(float lo, float hi) { f32x2_t v = {lo, hi}; bf16x2_t b = __builtin_convertvector(v, bf16x2_t); return __builtin_bit_cast(unsigned, b); }
; #define LAS __attribute__((address_space(3)))
; __device__ __forceinline__ float bflo(unsigned w) { return __uint_as_float(w << 16); }
; __device__ __forceinline__ float bfhi(unsigned w) { return __uint_as_float(w & 0xffff0000u); }
; __device__ __forceinline__ int v_st(int k, int c) { const int kk = (k & ~0xC) | ((k & 4) << 1) | ((k & 8) >> 1); return ((kk >> 3) * 4 + (c >> 5)) * 512 + ((kk & 7) * 32 + (c & 31)) * 2; }
; __device__ __forceinline__ void unit(const bf16_t* proj, const float* stats  , const float* lng, const float* lnb, const float* sw, const float* sb, bf16_t* Y2, int un, LAS unsigned char* lds) {
;     ...
;       for (int q = 0; q < 4; ++q) { const int s = sr + 32 * q, row = R0 + s; const u32x4 vv = *(const u32x4*)(proj + (size_t)row * NC + C_VC + ch);
;           const float mu = mus[q], rs = rss[q];
;           u32x4 w; w.x = pg8::cvt_pk_bf16((bflo(vv.x) - mu) * rs * g0[0] + b0[0], (bfhi(vv.x) - mu) * rs * g0[1] + b0[1]); w.y = pg8::cvt_pk_bf16((bflo(vv.y) - mu) * rs * g0[2] + b0[2], (bfhi(vv.y) - mu) * rs * g0[3] + b0[3]);
;           w.z = pg8::cvt_pk_bf16((bflo(vv.z) - mu) * rs * g1[0] + b1[0], (bfhi(vv.z) - mu) * rs * g1[1] + b1[1]); w.w = pg8::cvt_pk_bf16((bflo(vv.w) - mu) * rs * g1[2] + b1[2], (bfhi(vv.w) - mu) * rs * g1[3] + b1[3]);
;           *(LAS u32x4*)(lds + (s >> 6) * att::SHM_V + att::v_st(s & 63, sc)) = w; } }
;     __syncthreads();
;     ...
;             for (int j = 0; j < 8; ++j) x[j] = (s0 + j <= t) ? x[j] : 0.f;
	v_lshlrev_b32_e32 v112, 16, v196
	v_and_b32_e32 v113, 0xffff0000, v196
	v_pk_add_f32 v[112:113], v[112:113], v[102:103] op_sel_hi:[1,0] neg_lo:[0,1] neg_hi:[0,1]
	s_nop 0
	v_pk_mul_f32 v[112:113], v[108:109], v[112:113] op_sel_hi:[0,1]
	v_pk_fma_f32 v[112:113], v[92:93], v[112:113], v[96:97]
	s_nop 0
	v_cvt_pk_bf16_f32 v196, v112, v113
	v_lshlrev_b32_e32 v112, 16, v197
	v_and_b32_e32 v113, 0xffff0000, v197
	v_pk_add_f32 v[112:113], v[112:113], v[102:103] op_sel_hi:[1,0] neg_lo:[0,1] neg_hi:[0,1]
	s_nop 0
	v_pk_mul_f32 v[112:113], v[108:109], v[112:113] op_sel_hi:[0,1]
	v_pk_fma_f32 v[112:113], v[94:95], v[112:113], v[98:99]
	s_nop 0
	v_cvt_pk_bf16_f32 v197, v112, v113
	v_lshlrev_b32_e32 v112, 16, v198
	v_and_b32_e32 v113, 0xffff0000, v198
	v_pk_add_f32 v[112:113], v[112:113], v[102:103] op_sel_hi:[1,0] neg_lo:[0,1] neg_hi:[0,1]
	s_nop 0
	v_pk_mul_f32 v[112:113], v[108:109], v[112:113] op_sel_hi:[0,1]
	v_pk_fma_f32 v[112:113], v[84:85], v[112:113], v[88:89]
	s_nop 0
	v_cvt_pk_bf16_f32 v198, v112, v113
	v_lshlrev_b32_e32 v112, 16, v199
	v_and_b32_e32 v113, 0xffff0000, v199
	v_pk_add_f32 v[102:103], v[112:113], v[102:103] op_sel_hi:[1,0] neg_lo:[0,1] neg_hi:[0,1]
	s_nop 0
	v_pk_mul_f32 v[102:103], v[108:109], v[102:103] op_sel_hi:[0,1]
	v_pk_fma_f32 v[102:103], v[86:87], v[102:103], v[90:91]
	v_add_u32_e32 v108, 0x60, v185
	v_cvt_pk_bf16_f32 v199, v102, v103
	v_lshlrev_b32_e32 v102, 8, v114
	v_and_b32_e32 v102, 0xffffc000, v102
	v_add3_u32 v102, 0, v102, v116
	v_add3_u32 v102, v102, v189, v190
	ds_write_b128 v102, v[196:199]
	v_add_u32_e32 v102, s11, v108
	v_mad_i64_i32 v[100:101], s[0:1], v102, s14, v[100:101]
	v_lshl_add_u64 v[100:101], v[100:101], 0, v[110:111]
	v_add_co_u32_e32 v100, vcc, s4, v100
	s_cselect_b64 s[0:1], -1, 0
	s_nop 0
	v_addc_co_u32_e32 v101, vcc, 0, v101, vcc
	global_load_dwordx4 v[100:103], v[100:101], off offset:2048
	v_cmp_le_u32_e32 vcc, v183, v182
	s_mov_b64 s[4:5], -1
	s_waitcnt vmcnt(0)
	v_lshlrev_b32_e32 v110, 16, v100
	v_and_b32_e32 v111, 0xffff0000, v100
	v_pk_add_f32 v[110:111], v[110:111], v[104:105] op_sel_hi:[1,0] neg_lo:[0,1] neg_hi:[0,1]
	v_cndmask_b32_e32 v32, 0, v32, vcc
	v_pk_mul_f32 v[110:111], v[106:107], v[110:111] op_sel_hi:[0,1]
	v_pk_fma_f32 v[92:93], v[92:93], v[110:111], v[96:97]
	v_lshlrev_b32_e32 v96, 16, v101
	v_and_b32_e32 v97, 0xffff0000, v101
	v_pk_add_f32 v[96:97], v[96:97], v[104:105] op_sel_hi:[1,0] neg_lo:[0,1] neg_hi:[0,1]
	v_cvt_pk_bf16_f32 v92, v92, v93
	v_pk_mul_f32 v[96:97], v[106:107], v[96:97] op_sel_hi:[0,1]
	v_pk_fma_f32 v[94:95], v[94:95], v[96:97], v[98:99]
	v_cmp_lt_u32_e32 vcc, v183, v182
	v_cvt_pk_bf16_f32 v93, v94, v95
	v_lshlrev_b32_e32 v94, 16, v102
	v_and_b32_e32 v95, 0xffff0000, v102
	v_pk_add_f32 v[94:95], v[94:95], v[104:105] op_sel_hi:[1,0] neg_lo:[0,1] neg_hi:[0,1]
	v_cndmask_b32_e32 v33, 0, v33, vcc
	v_pk_mul_f32 v[94:95], v[106:107], v[94:95] op_sel_hi:[0,1]
	v_pk_fma_f32 v[84:85], v[84:85], v[94:95], v[88:89]
	s_nop 0
	v_cvt_pk_bf16_f32 v94, v84, v85
	v_lshlrev_b32_e32 v84, 16, v103
	v_and_b32_e32 v85, 0xffff0000, v103
	v_pk_add_f32 v[84:85], v[84:85], v[104:105] op_sel_hi:[1,0] neg_lo:[0,1] neg_hi:[0,1]
	s_nop 0
	v_pk_mul_f32 v[84:85], v[106:107], v[84:85] op_sel_hi:[0,1]
	v_pk_fma_f32 v[84:85], v[86:87], v[84:85], v[90:91]
	v_and_b32_e32 v86, 0xc0, v186
	v_cvt_pk_bf16_f32 v95, v84, v85
	v_and_or_b32 v85, v108, 48, v187
	v_lshrrev_b32_e32 v85, 1, v85
	v_lshlrev_b32_e32 v84, 8, v108
	v_or_b32_e32 v85, v85, v188
	v_and_b32_e32 v84, 0xffffc000, v84
	v_lshlrev_b32_e32 v85, 9, v85
	v_add3_u32 v84, 0, v84, v85
	v_add3_u32 v84, v84, v189, v190
	ds_write_b128 v84, v[92:95]
	v_lshlrev_b32_e32 v84, 3, v184
	v_and_b32_e32 v85, 24, v84
	v_lshlrev_b32_e32 v87, 1, v176
	v_and_b32_e32 v87, 32, v87
	v_and_b32_e32 v84, 0x100, v84
	v_add3_u32 v85, 0, v85, v86
	v_add3_u32 v100, v85, v87, v84
	v_or_b32_e32 v84, 2, v183
	v_cmp_le_u32_e32 vcc, v84, v182
	v_or_b32_e32 v84, 3, v183
	s_waitcnt lgkmcnt(0)
	v_cndmask_b32_e32 v34, 0, v34, vcc
	v_cmp_le_u32_e32 vcc, v84, v182
	v_or_b32_e32 v84, 4, v183
	s_barrier
; __device__ __forceinline__ unsigned cvt_pk_bf16(float lo, float hi) { f32x2_t v = {lo, hi}; bf16x2_t b = __builtin_convertvector(v, bf16x2_t); return __builtin_bit_cast(unsigned, b); }
; __device__ __forceinline__ void unit(const bf16_t* proj, const float* stats  , const float* lng, const float* lnb, const float* sw, const float* sb, bf16_t* Y2, int un, LAS unsigned char* lds) {
;     ...
;         if (st * 64 > tb * 32 + 31) continue;
;         att::bf16x8 pa[4];
; #pragma unroll
;         for (int k = 0; k < 4; ++k) { const int s0 = st * 64 + 16 * k + hi * 8; const f32x4 w0 = wv[2 * (st * 4 + k)], w1 = wv[2 * (st * 4 + k) + 1];
;             float x[8] = {w0[0], w0[1], w0[2], w0[3], w1[0], w1[1], w1[2], w1[3]};
; #pragma unroll
;             for (int j = 0; j < 8; ++j) x[j] = (s0 + j <= t) ? x[j] : 0.f;
;             u32x4 p; p.x = pg8::cvt_pk_bf16(x[0], x[1]); p.y = pg8::cvt_pk_bf16(x[2], x[3]); p.z = pg8::cvt_pk_bf16(x[4], x[5]); p.w = pg8::cvt_pk_bf16(x[6], x[7]); pa[k] = __builtin_bit_cast(att::bf16x8, p); }
;         if (eh == 0) { att::pv_one<0>(o0, vb + st * att::SHM_V, pa[0], pa[1], pa[2], pa[3]); att::pv_one<1>(o1, vb + st * att::SHM_V, pa[0], pa[1], pa[2], pa[3]); }
;         else         { att::pv_one<2>(o0, vb + st * att::SHM_V, pa[0], pa[1], pa[2], pa[3]); att::pv_one<3>(o1, vb + st * att::SHM_V, pa[0], pa[1], pa[2], pa[3]); }
	v_cndmask_b32_e32 v35, 0, v35, vcc
	v_cmp_le_u32_e32 vcc, v84, v182
	v_or_b32_e32 v84, 5, v183
	v_cvt_pk_bf16_f32 v85, v34, v35
	v_cndmask_b32_e32 v28, 0, v28, vcc
	v_cmp_le_u32_e32 vcc, v84, v182
	v_or_b32_e32 v84, 6, v183
	s_nop 0
	v_cndmask_b32_e32 v29, 0, v29, vcc
	v_cmp_le_u32_e32 vcc, v84, v182
	v_or_b32_e32 v84, 7, v183
	v_cvt_pk_bf16_f32 v86, v28, v29
	v_cndmask_b32_e32 v30, 0, v30, vcc
	v_cmp_le_u32_e32 vcc, v84, v182
	v_or_b32_e32 v28, 16, v183
	v_cvt_pk_bf16_f32 v84, v32, v33
	v_cndmask_b32_e32 v31, 0, v31, vcc
	v_cmp_le_u32_e32 vcc, v28, v182
	v_or_b32_e32 v28, 17, v183
	v_cvt_pk_bf16_f32 v87, v30, v31
	v_cndmask_b32_e32 v24, 0, v24, vcc
	v_cmp_le_u32_e32 vcc, v28, v182
	v_or_b32_e32 v28, 18, v183
	s_nop 0
	v_cndmask_b32_e32 v25, 0, v25, vcc
	v_cmp_le_u32_e32 vcc, v28, v182
	v_or_b32_e32 v28, 19, v183
	v_cvt_pk_bf16_f32 v88, v24, v25
	v_cndmask_b32_e32 v26, 0, v26, vcc
	v_cmp_le_u32_e32 vcc, v28, v182
	v_or_b32_e32 v28, 20, v183
	s_nop 0
	v_cndmask_b32_e32 v27, 0, v27, vcc
	v_cmp_le_u32_e32 vcc, v28, v182
	v_or_b32_e32 v28, 21, v183
	v_cvt_pk_bf16_f32 v89, v26, v27
	v_cndmask_b32_e32 v20, 0, v20, vcc
	v_cmp_le_u32_e32 vcc, v28, v182
	v_or_b32_e32 v28, 22, v183
	s_nop 0
	v_cndmask_b32_e32 v21, 0, v21, vcc
	v_cmp_le_u32_e32 vcc, v28, v182
	v_or_b32_e32 v28, 23, v183
	v_cvt_pk_bf16_f32 v90, v20, v21
	v_cndmask_b32_e32 v22, 0, v22, vcc
	v_cmp_le_u32_e32 vcc, v28, v182
	v_or_b32_e32 v20, 32, v183
	s_nop 0
	v_cndmask_b32_e32 v23, 0, v23, vcc
	v_cmp_le_u32_e32 vcc, v20, v182
	v_or_b32_e32 v20, 33, v183
	v_cvt_pk_bf16_f32 v91, v22, v23
	v_cndmask_b32_e32 v16, 0, v16, vcc
	v_cmp_le_u32_e32 vcc, v20, v182
	v_or_b32_e32 v20, 34, v183
	s_nop 0
	v_cndmask_b32_e32 v17, 0, v17, vcc
	v_cmp_le_u32_e32 vcc, v20, v182
	v_or_b32_e32 v20, 35, v183
	v_cvt_pk_bf16_f32 v96, v16, v17
	v_cndmask_b32_e32 v18, 0, v18, vcc
	v_cmp_le_u32_e32 vcc, v20, v182
	v_or_b32_e32 v20, 36, v183
	s_nop 0
	v_cndmask_b32_e32 v19, 0, v19, vcc
	v_cmp_le_u32_e32 vcc, v20, v182
	v_or_b32_e32 v20, 37, v183
	v_cvt_pk_bf16_f32 v97, v18, v19
	v_cndmask_b32_e32 v12, 0, v12, vcc
	v_cmp_le_u32_e32 vcc, v20, v182
	v_or_b32_e32 v20, 38, v183
	s_nop 0
	v_cndmask_b32_e32 v13, 0, v13, vcc
	v_cmp_le_u32_e32 vcc, v20, v182
	v_or_b32_e32 v20, 39, v183
	v_cvt_pk_bf16_f32 v98, v12, v13
	v_cndmask_b32_e32 v14, 0, v14, vcc
	v_cmp_le_u32_e32 vcc, v20, v182
	v_or_b32_e32 v12, 48, v183
	s_nop 0
	v_cndmask_b32_e32 v15, 0, v15, vcc
	v_cmp_le_u32_e32 vcc, v12, v182
	v_or_b32_e32 v12, 49, v183
	v_cvt_pk_bf16_f32 v99, v14, v15
	v_cndmask_b32_e32 v8, 0, v8, vcc
	v_cmp_le_u32_e32 vcc, v12, v182
	v_or_b32_e32 v12, 50, v183
	s_nop 0
	v_cndmask_b32_e32 v9, 0, v9, vcc
	v_cmp_le_u32_e32 vcc, v12, v182
	v_or_b32_e32 v12, 51, v183
	v_cvt_pk_bf16_f32 v92, v8, v9
	v_cndmask_b32_e32 v10, 0, v10, vcc
	v_cmp_le_u32_e32 vcc, v12, v182
	v_or_b32_e32 v12, 52, v183
	s_nop 0
	v_cndmask_b32_e32 v11, 0, v11, vcc
	v_cmp_le_u32_e32 vcc, v12, v182
	v_or_b32_e32 v12, 53, v183
	v_cvt_pk_bf16_f32 v93, v10, v11
	v_cndmask_b32_e32 v4, 0, v4, vcc
	v_cmp_le_u32_e32 vcc, v12, v182
	v_or_b32_e32 v12, 54, v183
	s_nop 0
	v_cndmask_b32_e32 v5, 0, v5, vcc
	v_cmp_le_u32_e32 vcc, v12, v182
	v_or_b32_e32 v12, 55, v183
	v_cvt_pk_bf16_f32 v94, v4, v5
	v_cndmask_b32_e32 v6, 0, v6, vcc
	v_cmp_le_u32_e32 vcc, v12, v182
	s_nop 1
	v_cndmask_b32_e32 v7, 0, v7, vcc
	v_cvt_pk_bf16_f32 v95, v6, v7
	s_and_b64 vcc, exec, s[0:1]
	s_cbranch_vccz .LBB0_1379
	ds_read_b64_tr_b16 v[4:5], v100 offset:1024
	ds_read_b64_tr_b16 v[6:7], v100 offset:3072
	ds_read_b64_tr_b16 v[20:21], v100 offset:5120
	ds_read_b64_tr_b16 v[22:23], v100 offset:7168
	s_mov_b64 s[4:5], 0
	s_waitcnt lgkmcnt(2)
	v_mfma_f32_32x32x16_bf16 v[4:19], v[84:87], v[4:7], 0
	s_waitcnt lgkmcnt(0)
	v_mfma_f32_32x32x16_bf16 v[4:19], v[88:91], v[20:23], v[4:19]
	ds_read_b64_tr_b16 v[20:21], v100 offset:9216
	ds_read_b64_tr_b16 v[22:23], v100 offset:11264
	s_waitcnt lgkmcnt(0)
	v_mfma_f32_32x32x16_bf16 v[4:19], v[96:99], v[20:23], v[4:19]
	ds_read_b64_tr_b16 v[20:21], v100 offset:13312
	ds_read_b64_tr_b16 v[22:23], v100 offset:15360
	s_waitcnt lgkmcnt(0)
	v_mfma_f32_32x32x16_bf16 v[4:19], v[92:95], v[20:23], v[4:19]
	ds_read_b64_tr_b16 v[22:23], v100 offset:3584
	ds_read_b64_tr_b16 v[20:21], v100 offset:1536
	ds_read_b64_tr_b16 v[104:105], v100 offset:7680
	ds_read_b64_tr_b16 v[102:103], v100 offset:5632
	s_waitcnt lgkmcnt(2)
	v_mfma_f32_32x32x16_bf16 v[20:35], v[84:87], v[20:23], 0
	s_waitcnt lgkmcnt(0)
	v_mfma_f32_32x32x16_bf16 v[20:35], v[88:91], v[102:105], v[20:35]
	ds_read_b64_tr_b16 v[104:105], v100 offset:11776
	ds_read_b64_tr_b16 v[102:103], v100 offset:9728
	s_waitcnt lgkmcnt(0)
	v_mfma_f32_32x32x16_bf16 v[20:35], v[96:99], v[102:105], v[20:35]
	ds_read_b64_tr_b16 v[104:105], v100 offset:15872
	ds_read_b64_tr_b16 v[102:103], v100 offset:13824
	s_waitcnt lgkmcnt(0)
	v_mfma_f32_32x32x16_bf16 v[20:35], v[92:95], v[102:105], v[20:35]
